# scale loads of the int8 GEMM units issued in the second load segment of the first K-tile pair (behind its four operand loads) instead of ahead of the first MFMA segment; counted waits 18 / 20
# speedup vs baseline: 1.0002x; 1.0002x over previous
.LBB0_531:
	s_waitcnt vmcnt(8)
	s_waitcnt lgkmcnt(0)
	s_barrier
	s_setprio 1
	v_mfma_i32_16x16x64_i8 v[18:21], v[158:161], v[190:193], 0
	s_nop 0
	v_mfma_i32_16x16x64_i8 v[18:21], v[154:157], v[186:189], v[18:21]
	v_mfma_i32_16x16x64_i8 v[22:25], v[150:153], v[190:193], 0
	s_nop 0
	v_mfma_i32_16x16x64_i8 v[22:25], v[142:145], v[186:189], v[22:25]
	v_mfma_i32_16x16x64_i8 v[26:29], v[146:149], v[190:193], 0
	s_nop 0
	v_mfma_i32_16x16x64_i8 v[26:29], v[138:141], v[186:189], v[26:29]
	v_mfma_i32_16x16x64_i8 v[34:37], v[134:137], v[190:193], 0
	s_nop 0
	v_mfma_i32_16x16x64_i8 v[34:37], v[130:133], v[186:189], v[34:37]
	v_mfma_i32_16x16x64_i8 v[50:53], v[158:161], v[182:185], 0
	s_nop 0
	v_mfma_i32_16x16x64_i8 v[50:53], v[154:157], v[178:181], v[50:53]
	v_mfma_i32_16x16x64_i8 v[62:65], v[150:153], v[182:185], 0
	s_nop 0
	v_mfma_i32_16x16x64_i8 v[62:65], v[142:145], v[178:181], v[62:65]
	v_mfma_i32_16x16x64_i8 v[54:57], v[146:149], v[182:185], 0
	s_nop 0
	v_mfma_i32_16x16x64_i8 v[54:57], v[138:141], v[178:181], v[54:57]
	v_mfma_i32_16x16x64_i8 v[66:69], v[134:137], v[182:185], 0
	s_nop 0
	v_mfma_i32_16x16x64_i8 v[66:69], v[130:133], v[178:181], v[66:69]
	v_mfma_i32_16x16x64_i8 v[82:85], v[158:161], v[174:177], 0
	s_nop 0
	v_mfma_i32_16x16x64_i8 v[82:85], v[154:157], v[170:173], v[82:85]
	v_mfma_i32_16x16x64_i8 v[94:97], v[150:153], v[174:177], 0
	s_nop 0
	v_mfma_i32_16x16x64_i8 v[94:97], v[142:145], v[170:173], v[94:97]
	v_mfma_i32_16x16x64_i8 v[86:89], v[146:149], v[174:177], 0
	s_nop 0
	v_mfma_i32_16x16x64_i8 v[86:89], v[138:141], v[170:173], v[86:89]
	v_mfma_i32_16x16x64_i8 v[98:101], v[134:137], v[174:177], 0
	s_nop 0
	v_mfma_i32_16x16x64_i8 v[98:101], v[130:133], v[170:173], v[98:101]
	v_mfma_i32_16x16x64_i8 v[114:117], v[158:161], v[166:169], 0
	s_nop 0
	v_mfma_i32_16x16x64_i8 v[114:117], v[154:157], v[162:165], v[114:117]
	v_mfma_i32_16x16x64_i8 v[122:125], v[150:153], v[166:169], 0
	s_nop 0
	v_mfma_i32_16x16x64_i8 v[122:125], v[142:145], v[162:165], v[122:125]
	v_mfma_i32_16x16x64_i8 v[118:121], v[146:149], v[166:169], 0
	s_nop 0
	v_mfma_i32_16x16x64_i8 v[118:121], v[138:141], v[162:165], v[118:121]
	v_mfma_i32_16x16x64_i8 v[126:129], v[134:137], v[166:169], 0
	s_nop 0
	v_mfma_i32_16x16x64_i8 v[126:129], v[130:133], v[162:165], v[126:129]
	s_setprio 0
	s_barrier
	s_add_u32 s63, s35, s66
	s_addc_u32 s69, s60, s67
	s_cmp_eq_u32 s49, 12
	s_cselect_b64 s[82:83], -1, 0
	s_and_b64 s[70:71], s[82:83], exec
	s_cselect_b32 s79, s79, s69
	s_cselect_b32 s78, s78, s63
	s_mov_b64 s[70:71], s[78:79]
	v_mov_b32_e32 v205, v197
	s_mov_b32 m0, s19
	s_waitcnt lgkmcnt(0)
	ds_read_b128 v[190:193], v204 offset:16384
	ds_read_b128 v[186:189], v204 offset:17408
	ds_read_b128 v[182:185], v204 offset:18432
	ds_read_b128 v[178:181], v204 offset:19456
	ds_read_b128 v[174:177], v204 offset:20480
	ds_read_b128 v[170:173], v204 offset:21504
	ds_read_b128 v[166:169], v204 offset:22528
	ds_read_b128 v[162:165], v204 offset:23552
	s_nop 0
	global_load_lds_dwordx4 v205, s[70:71]
	v_mov_b32_e32 v205, v199
	s_mov_b32 m0, s20
	s_nop 0
	global_load_lds_dwordx4 v205, s[70:71]
	s_add_u32 s70, s78, 0x40000
	s_addc_u32 s71, s79, 0
	v_mov_b32_e32 v205, v197
	s_mov_b32 m0, s21
	s_nop 0
	global_load_lds_dwordx4 v205, s[70:71]
	v_mov_b32_e32 v205, v199
	s_mov_b32 m0, s22
	s_nop 0
	global_load_lds_dwordx4 v205, s[70:71]
	v_lshl_or_b32 v242, s61, 8, v203
	v_lshl_add_u32 v240, s33, 8, v201
	v_ashrrev_i32_e32 v243, 31, v242
	v_ashrrev_i32_e32 v241, 31, v240
	v_lshl_add_u64 v[242:243], v[242:243], 2, s[6:7]
	v_lshl_add_u64 v[240:241], v[240:241], 2, s[38:39]
	global_load_dwordx4 v[210:213], v[242:243], off
	global_load_dwordx4 v[214:217], v[242:243], off offset:16
	global_load_dwordx4 v[218:221], v[242:243], off offset:512
	global_load_dwordx4 v[222:225], v[242:243], off offset:528
	global_load_dword v232, v[240:241], off
	global_load_dword v233, v[240:241], off offset:64
	global_load_dword v234, v[240:241], off offset:128
	global_load_dword v235, v[240:241], off offset:192
	global_load_dword v236, v[240:241], off offset:512
	global_load_dword v237, v[240:241], off offset:576
	global_load_dword v238, v[240:241], off offset:640
	global_load_dword v239, v[240:241], off offset:704
	s_waitcnt vmcnt(18)
	s_waitcnt lgkmcnt(0)
	s_barrier
	s_setprio 1
	v_mfma_i32_16x16x64_i8 v[2:5], v[158:161], v[190:193], 0
	s_nop 0
	v_mfma_i32_16x16x64_i8 v[2:5], v[154:157], v[186:189], v[2:5]
	v_mfma_i32_16x16x64_i8 v[6:9], v[150:153], v[190:193], 0
	s_nop 0
	v_mfma_i32_16x16x64_i8 v[6:9], v[142:145], v[186:189], v[6:9]
	v_mfma_i32_16x16x64_i8 v[10:13], v[146:149], v[190:193], 0
	s_nop 0
	v_mfma_i32_16x16x64_i8 v[10:13], v[138:141], v[186:189], v[10:13]
	v_mfma_i32_16x16x64_i8 v[14:17], v[134:137], v[190:193], 0
	s_nop 0
	v_mfma_i32_16x16x64_i8 v[14:17], v[130:133], v[186:189], v[14:17]
	v_mfma_i32_16x16x64_i8 v[30:33], v[158:161], v[182:185], 0
	s_nop 0
	v_mfma_i32_16x16x64_i8 v[30:33], v[154:157], v[178:181], v[30:33]
	v_mfma_i32_16x16x64_i8 v[42:45], v[150:153], v[182:185], 0
	s_nop 0
	v_mfma_i32_16x16x64_i8 v[42:45], v[142:145], v[178:181], v[42:45]
	v_mfma_i32_16x16x64_i8 v[38:41], v[146:149], v[182:185], 0
	s_nop 0
	v_mfma_i32_16x16x64_i8 v[38:41], v[138:141], v[178:181], v[38:41]
	v_mfma_i32_16x16x64_i8 v[46:49], v[134:137], v[182:185], 0
	s_nop 0
	v_mfma_i32_16x16x64_i8 v[46:49], v[130:133], v[178:181], v[46:49]
	v_mfma_i32_16x16x64_i8 v[58:61], v[158:161], v[174:177], 0
	s_nop 0
	v_mfma_i32_16x16x64_i8 v[58:61], v[154:157], v[170:173], v[58:61]
	v_mfma_i32_16x16x64_i8 v[74:77], v[150:153], v[174:177], 0
	s_nop 0
	v_mfma_i32_16x16x64_i8 v[74:77], v[142:145], v[170:173], v[74:77]
	v_mfma_i32_16x16x64_i8 v[70:73], v[146:149], v[174:177], 0
	s_nop 0
	v_mfma_i32_16x16x64_i8 v[70:73], v[138:141], v[170:173], v[70:73]
	v_mfma_i32_16x16x64_i8 v[78:81], v[134:137], v[174:177], 0
	s_nop 0
	v_mfma_i32_16x16x64_i8 v[78:81], v[130:133], v[170:173], v[78:81]
	v_mfma_i32_16x16x64_i8 v[90:93], v[158:161], v[166:169], 0
	s_nop 0
	v_mfma_i32_16x16x64_i8 v[90:93], v[154:157], v[162:165], v[90:93]
	v_mfma_i32_16x16x64_i8 v[106:109], v[150:153], v[166:169], 0
	s_nop 0
	v_mfma_i32_16x16x64_i8 v[106:109], v[142:145], v[162:165], v[106:109]
	v_mfma_i32_16x16x64_i8 v[102:105], v[146:149], v[166:169], 0
	s_nop 0
	v_mfma_i32_16x16x64_i8 v[102:105], v[138:141], v[162:165], v[102:105]
	v_mfma_i32_16x16x64_i8 v[110:113], v[134:137], v[166:169], 0
	s_nop 0
	v_mfma_i32_16x16x64_i8 v[110:113], v[130:133], v[162:165], v[110:113]
	s_setprio 0
	s_barrier
	s_add_u32 s51, s51, 0x100
	s_addc_u32 s69, s62, 0
	s_and_b64 s[62:63], s[82:83], exec
	s_cselect_b32 s63, s77, s69
	s_cselect_b32 s62, s76, s51
	s_add_u32 s76, s78, 0x80
	s_addc_u32 s77, s79, 0
	s_add_i32 s51, 0, 0x18000
	s_add_i32 s69, 0, 0x1c000
	v_add_u32_e32 v130, s51, v202
	v_add_u32_e32 v131, s69, v202
	ds_read_b128 v[158:161], v130
	ds_read_b128 v[154:157], v130 offset:1024
	ds_read_b128 v[150:153], v130 offset:2048
	ds_read_b128 v[146:149], v130 offset:3072
	ds_read_b128 v[142:145], v131
	ds_read_b128 v[138:141], v131 offset:1024
	ds_read_b128 v[134:137], v131 offset:2048
	ds_read_b128 v[130:133], v131 offset:3072
	s_mov_b64 s[70:71], s[62:63]
	v_mov_b32_e32 v205, v196
	s_mov_b32 m0, s1
	s_waitcnt lgkmcnt(0)
	ds_read_b128 v[162:165], v204 offset:32768
	ds_read_b128 v[166:169], v204 offset:33792
	ds_read_b128 v[170:173], v204 offset:34816
	ds_read_b128 v[174:177], v204 offset:35840
	ds_read_b128 v[178:181], v204 offset:36864
	ds_read_b128 v[182:185], v204 offset:37888
	ds_read_b128 v[186:189], v204 offset:38912
	ds_read_b128 v[190:193], v204 offset:39936
	s_add_u32 s62, s62, 0x40000
	global_load_lds_dwordx4 v205, s[70:71]
	v_mov_b32_e32 v205, v198
	s_mov_b32 m0, s23
	s_addc_u32 s63, s63, 0
	global_load_lds_dwordx4 v205, s[70:71]
	v_mov_b32_e32 v205, v196
	s_mov_b32 m0, s26
	s_nop 0
	global_load_lds_dwordx4 v205, s[62:63]
	v_mov_b32_e32 v205, v198
	s_mov_b32 m0, s27
	s_nop 0
	global_load_lds_dwordx4 v205, s[62:63]
	s_waitcnt vmcnt(20)
	s_waitcnt lgkmcnt(0)
	s_barrier
	s_setprio 1
	s_waitcnt lgkmcnt(0)
	v_mfma_i32_16x16x64_i8 v[18:21], v[158:161], v[162:165], v[18:21]
	s_nop 0
	v_mfma_i32_16x16x64_i8 v[18:21], v[154:157], v[166:169], v[18:21]
	v_mfma_i32_16x16x64_i8 v[22:25], v[150:153], v[162:165], v[22:25]
	s_nop 0
	v_mfma_i32_16x16x64_i8 v[22:25], v[146:149], v[166:169], v[22:25]
	v_mfma_i32_16x16x64_i8 v[26:29], v[142:145], v[162:165], v[26:29]
	s_nop 0
	v_mfma_i32_16x16x64_i8 v[26:29], v[138:141], v[166:169], v[26:29]
	v_mfma_i32_16x16x64_i8 v[34:37], v[134:137], v[162:165], v[34:37]
	s_nop 0
	v_mfma_i32_16x16x64_i8 v[34:37], v[130:133], v[166:169], v[34:37]
	v_mfma_i32_16x16x64_i8 v[50:53], v[158:161], v[170:173], v[50:53]
	s_nop 0
	v_mfma_i32_16x16x64_i8 v[50:53], v[154:157], v[174:177], v[50:53]
	v_mfma_i32_16x16x64_i8 v[62:65], v[150:153], v[170:173], v[62:65]
	s_nop 0
	v_mfma_i32_16x16x64_i8 v[62:65], v[146:149], v[174:177], v[62:65]
	v_mfma_i32_16x16x64_i8 v[54:57], v[142:145], v[170:173], v[54:57]
	s_nop 0
	v_mfma_i32_16x16x64_i8 v[54:57], v[138:141], v[174:177], v[54:57]
	v_mfma_i32_16x16x64_i8 v[66:69], v[134:137], v[170:173], v[66:69]
	s_nop 0
	v_mfma_i32_16x16x64_i8 v[66:69], v[130:133], v[174:177], v[66:69]
	v_mfma_i32_16x16x64_i8 v[82:85], v[158:161], v[178:181], v[82:85]
	s_nop 0
	v_mfma_i32_16x16x64_i8 v[82:85], v[154:157], v[182:185], v[82:85]
	v_mfma_i32_16x16x64_i8 v[94:97], v[150:153], v[178:181], v[94:97]
	s_nop 0
	v_mfma_i32_16x16x64_i8 v[94:97], v[146:149], v[182:185], v[94:97]
	v_mfma_i32_16x16x64_i8 v[86:89], v[142:145], v[178:181], v[86:89]
	s_nop 0
	v_mfma_i32_16x16x64_i8 v[86:89], v[138:141], v[182:185], v[86:89]
	v_mfma_i32_16x16x64_i8 v[98:101], v[134:137], v[178:181], v[98:101]
	s_nop 0
	v_mfma_i32_16x16x64_i8 v[98:101], v[130:133], v[182:185], v[98:101]
	v_mfma_i32_16x16x64_i8 v[114:117], v[158:161], v[186:189], v[114:117]
	s_nop 0
	v_mfma_i32_16x16x64_i8 v[114:117], v[154:157], v[190:193], v[114:117]
	v_mfma_i32_16x16x64_i8 v[122:125], v[150:153], v[186:189], v[122:125]
	s_nop 0
	v_mfma_i32_16x16x64_i8 v[122:125], v[146:149], v[190:193], v[122:125]
	v_mfma_i32_16x16x64_i8 v[118:121], v[142:145], v[186:189], v[118:121]
	s_nop 0
	v_mfma_i32_16x16x64_i8 v[118:121], v[138:141], v[190:193], v[118:121]
	v_mfma_i32_16x16x64_i8 v[126:129], v[134:137], v[186:189], v[126:129]
	s_nop 0
	v_mfma_i32_16x16x64_i8 v[126:129], v[130:133], v[190:193], v[126:129]
	s_setprio 0
	s_barrier
	v_mov_b32_e32 v205, v197
	s_add_i32 s51, s51, s10
	ds_read_b128 v[162:165], v204 offset:49152
	ds_read_b128 v[166:169], v204 offset:50176
	ds_read_b128 v[170:173], v204 offset:51200
	ds_read_b128 v[174:177], v204 offset:52224
	ds_read_b128 v[178:181], v204 offset:53248
	ds_read_b128 v[182:185], v204 offset:54272
	ds_read_b128 v[186:189], v204 offset:55296
	ds_read_b128 v[190:193], v204 offset:56320
	s_mov_b32 m0, s51
	s_nop 0
	global_load_lds_dwordx4 v205, s[76:77]
	v_mov_b32_e32 v205, v199
	s_add_i32 m0, s51, 0x2000
	s_add_u32 s62, s78, 0x40080
	global_load_lds_dwordx4 v205, s[76:77]
	s_addc_u32 s63, s79, 0
	v_mov_b32_e32 v205, v197
	s_add_i32 s51, s69, s10
	s_mov_b32 m0, s51
	s_nop 0
	global_load_lds_dwordx4 v205, s[62:63]
	v_mov_b32_e32 v205, v199
	s_add_i32 m0, s51, 0x2000
	s_nop 0
	global_load_lds_dwordx4 v205, s[62:63]
	s_waitcnt vmcnt(6)
	s_waitcnt lgkmcnt(0)
	s_barrier
	s_setprio 1
	s_waitcnt lgkmcnt(0)
	v_mfma_i32_16x16x64_i8 v[2:5], v[158:161], v[162:165], v[2:5]
	s_nop 0
	v_mfma_i32_16x16x64_i8 v[2:5], v[154:157], v[166:169], v[2:5]
	v_mfma_i32_16x16x64_i8 v[6:9], v[150:153], v[162:165], v[6:9]
	s_nop 0
	v_mfma_i32_16x16x64_i8 v[6:9], v[146:149], v[166:169], v[6:9]
	v_mfma_i32_16x16x64_i8 v[10:13], v[142:145], v[162:165], v[10:13]
	s_nop 0
	v_mfma_i32_16x16x64_i8 v[10:13], v[138:141], v[166:169], v[10:13]
	v_mfma_i32_16x16x64_i8 v[14:17], v[134:137], v[162:165], v[14:17]
	s_nop 0
	v_mfma_i32_16x16x64_i8 v[14:17], v[130:133], v[166:169], v[14:17]
	v_mfma_i32_16x16x64_i8 v[30:33], v[158:161], v[170:173], v[30:33]
	s_nop 0
	v_mfma_i32_16x16x64_i8 v[30:33], v[154:157], v[174:177], v[30:33]
	v_mfma_i32_16x16x64_i8 v[42:45], v[150:153], v[170:173], v[42:45]
	s_nop 0
	v_mfma_i32_16x16x64_i8 v[42:45], v[146:149], v[174:177], v[42:45]
	v_mfma_i32_16x16x64_i8 v[38:41], v[142:145], v[170:173], v[38:41]
	s_nop 0
	v_mfma_i32_16x16x64_i8 v[38:41], v[138:141], v[174:177], v[38:41]
	v_mfma_i32_16x16x64_i8 v[46:49], v[134:137], v[170:173], v[46:49]
	s_nop 0
	v_mfma_i32_16x16x64_i8 v[46:49], v[130:133], v[174:177], v[46:49]
	v_mfma_i32_16x16x64_i8 v[58:61], v[158:161], v[178:181], v[58:61]
	s_nop 0
	v_mfma_i32_16x16x64_i8 v[58:61], v[154:157], v[182:185], v[58:61]
	v_mfma_i32_16x16x64_i8 v[74:77], v[150:153], v[178:181], v[74:77]
	s_nop 0
	v_mfma_i32_16x16x64_i8 v[74:77], v[146:149], v[182:185], v[74:77]
	v_mfma_i32_16x16x64_i8 v[70:73], v[142:145], v[178:181], v[70:73]
	s_nop 0
	v_mfma_i32_16x16x64_i8 v[70:73], v[138:141], v[182:185], v[70:73]
	v_mfma_i32_16x16x64_i8 v[78:81], v[134:137], v[178:181], v[78:81]
	s_nop 0
	v_mfma_i32_16x16x64_i8 v[78:81], v[130:133], v[182:185], v[78:81]
	v_mfma_i32_16x16x64_i8 v[90:93], v[158:161], v[186:189], v[90:93]
	s_nop 0
	v_mfma_i32_16x16x64_i8 v[90:93], v[154:157], v[190:193], v[90:93]
	v_mfma_i32_16x16x64_i8 v[106:109], v[150:153], v[186:189], v[106:109]
	s_nop 0
	v_mfma_i32_16x16x64_i8 v[106:109], v[146:149], v[190:193], v[106:109]
	v_mfma_i32_16x16x64_i8 v[102:105], v[142:145], v[186:189], v[102:105]
	s_nop 0
	v_mfma_i32_16x16x64_i8 v[102:105], v[138:141], v[190:193], v[102:105]
	v_mfma_i32_16x16x64_i8 v[110:113], v[134:137], v[186:189], v[110:113]
	s_nop 0
	v_mfma_i32_16x16x64_i8 v[110:113], v[130:133], v[190:193], v[110:113]
	s_setprio 0
	s_barrier
	s_add_i32 s49, s49, 2
	s_add_u32 s66, s66, 0x100
	s_addc_u32 s67, s67, 0
	s_cmp_gt_u32 s49, 13
	s_cbranch_scc1 .LBB0_541
	s_mov_b64 s[78:79], s[8:9]
	s_mov_b64 s[76:77], s[40:41]

.LBB0_851:
	s_waitcnt vmcnt(8)
	s_waitcnt lgkmcnt(0)
	s_barrier
	s_setprio 1
	v_mfma_i32_16x16x64_i8 v[18:21], v[158:161], v[190:193], 0
	s_nop 0
	v_mfma_i32_16x16x64_i8 v[18:21], v[154:157], v[186:189], v[18:21]
	v_mfma_i32_16x16x64_i8 v[22:25], v[150:153], v[190:193], 0
	s_nop 0
	v_mfma_i32_16x16x64_i8 v[22:25], v[142:145], v[186:189], v[22:25]
	v_mfma_i32_16x16x64_i8 v[26:29], v[146:149], v[190:193], 0
	s_nop 0
	v_mfma_i32_16x16x64_i8 v[26:29], v[138:141], v[186:189], v[26:29]
	v_mfma_i32_16x16x64_i8 v[34:37], v[134:137], v[190:193], 0
	s_nop 0
	v_mfma_i32_16x16x64_i8 v[34:37], v[130:133], v[186:189], v[34:37]
	v_mfma_i32_16x16x64_i8 v[50:53], v[158:161], v[182:185], 0
	s_nop 0
	v_mfma_i32_16x16x64_i8 v[50:53], v[154:157], v[178:181], v[50:53]
	v_mfma_i32_16x16x64_i8 v[62:65], v[150:153], v[182:185], 0
	s_nop 0
	v_mfma_i32_16x16x64_i8 v[62:65], v[142:145], v[178:181], v[62:65]
	v_mfma_i32_16x16x64_i8 v[54:57], v[146:149], v[182:185], 0
	s_nop 0
	v_mfma_i32_16x16x64_i8 v[54:57], v[138:141], v[178:181], v[54:57]
	v_mfma_i32_16x16x64_i8 v[66:69], v[134:137], v[182:185], 0
	s_nop 0
	v_mfma_i32_16x16x64_i8 v[66:69], v[130:133], v[178:181], v[66:69]
	v_mfma_i32_16x16x64_i8 v[82:85], v[158:161], v[174:177], 0
	s_nop 0
	v_mfma_i32_16x16x64_i8 v[82:85], v[154:157], v[170:173], v[82:85]
	v_mfma_i32_16x16x64_i8 v[94:97], v[150:153], v[174:177], 0
	s_nop 0
	v_mfma_i32_16x16x64_i8 v[94:97], v[142:145], v[170:173], v[94:97]
	v_mfma_i32_16x16x64_i8 v[86:89], v[146:149], v[174:177], 0
	s_nop 0
	v_mfma_i32_16x16x64_i8 v[86:89], v[138:141], v[170:173], v[86:89]
	v_mfma_i32_16x16x64_i8 v[98:101], v[134:137], v[174:177], 0
	s_nop 0
	v_mfma_i32_16x16x64_i8 v[98:101], v[130:133], v[170:173], v[98:101]
	v_mfma_i32_16x16x64_i8 v[114:117], v[158:161], v[166:169], 0
	s_nop 0
	v_mfma_i32_16x16x64_i8 v[114:117], v[154:157], v[162:165], v[114:117]
	v_mfma_i32_16x16x64_i8 v[122:125], v[150:153], v[166:169], 0
	s_nop 0
	v_mfma_i32_16x16x64_i8 v[122:125], v[142:145], v[162:165], v[122:125]
	v_mfma_i32_16x16x64_i8 v[118:121], v[146:149], v[166:169], 0
	s_nop 0
	v_mfma_i32_16x16x64_i8 v[118:121], v[138:141], v[162:165], v[118:121]
	v_mfma_i32_16x16x64_i8 v[126:129], v[134:137], v[166:169], 0
	s_nop 0
	v_mfma_i32_16x16x64_i8 v[126:129], v[130:133], v[162:165], v[126:129]
	s_setprio 0
	s_barrier
	s_add_u32 s81, s74, s50
	s_addc_u32 s82, s75, s51
	s_cmp_eq_u32 s43, 12
	s_cselect_b64 s[76:77], -1, 0
	s_and_b64 s[78:79], s[76:77], exec
	s_cselect_b32 s65, s65, s82
	s_cselect_b32 s64, s64, s81
	s_mov_b64 s[78:79], s[64:65]
	v_mov_b32_e32 v209, v202
	s_mov_b32 m0, s21
	s_waitcnt lgkmcnt(0)
	ds_read_b128 v[190:193], v207 offset:16384
	ds_read_b128 v[186:189], v207 offset:17408
	ds_read_b128 v[182:185], v207 offset:18432
	ds_read_b128 v[178:181], v207 offset:19456
	ds_read_b128 v[174:177], v207 offset:20480
	ds_read_b128 v[170:173], v207 offset:21504
	ds_read_b128 v[166:169], v207 offset:22528
	ds_read_b128 v[162:165], v207 offset:23552
	s_nop 0
	global_load_lds_dwordx4 v209, s[78:79]
	v_mov_b32_e32 v209, v204
	s_mov_b32 m0, s33
	s_nop 0
	global_load_lds_dwordx4 v209, s[78:79]
	s_add_u32 s78, s64, 0x40000
	s_addc_u32 s79, s65, 0
	v_mov_b32_e32 v209, v202
	s_mov_b32 m0, s35
	s_nop 0
	global_load_lds_dwordx4 v209, s[78:79]
	v_mov_b32_e32 v209, v204
	s_mov_b32 m0, s60
	s_nop 0
	global_load_lds_dwordx4 v209, s[78:79]
	s_mul_i32 s100, s73, 0x100
	s_mov_b32 s101, 0
	v_lshl_add_u32 v240, s72, 8, v205
	v_ashrrev_i32_e32 v241, 31, v240
	v_lshl_add_u64 v[242:243], s[100:101], 2, v[194:195]
	v_lshl_add_u64 v[240:241], v[240:241], 2, s[38:39]
	global_load_dwordx4 v[210:213], v[242:243], off
	global_load_dwordx4 v[214:217], v[242:243], off offset:16
	global_load_dwordx4 v[218:221], v[242:243], off offset:528
	global_load_dwordx4 v[222:225], v[242:243], off offset:512
	global_load_dword v232, v[240:241], off
	global_load_dword v233, v[240:241], off offset:64
	global_load_dword v234, v[240:241], off offset:128
	global_load_dword v235, v[240:241], off offset:192
	global_load_dword v236, v[240:241], off offset:512
	global_load_dword v237, v[240:241], off offset:576
	global_load_dword v238, v[240:241], off offset:640
	global_load_dword v239, v[240:241], off offset:704
	s_waitcnt vmcnt(18)
	s_waitcnt lgkmcnt(0)
	s_barrier
	s_setprio 1
	v_mfma_i32_16x16x64_i8 v[2:5], v[158:161], v[190:193], 0
	s_nop 0
	v_mfma_i32_16x16x64_i8 v[2:5], v[154:157], v[186:189], v[2:5]
	v_mfma_i32_16x16x64_i8 v[6:9], v[150:153], v[190:193], 0
	s_nop 0
	v_mfma_i32_16x16x64_i8 v[6:9], v[142:145], v[186:189], v[6:9]
	v_mfma_i32_16x16x64_i8 v[10:13], v[146:149], v[190:193], 0
	s_nop 0
	v_mfma_i32_16x16x64_i8 v[10:13], v[138:141], v[186:189], v[10:13]
	v_mfma_i32_16x16x64_i8 v[14:17], v[134:137], v[190:193], 0
	s_nop 0
	v_mfma_i32_16x16x64_i8 v[14:17], v[130:133], v[186:189], v[14:17]
	v_mfma_i32_16x16x64_i8 v[30:33], v[158:161], v[182:185], 0
	s_nop 0
	v_mfma_i32_16x16x64_i8 v[30:33], v[154:157], v[178:181], v[30:33]
	v_mfma_i32_16x16x64_i8 v[42:45], v[150:153], v[182:185], 0
	s_nop 0
	v_mfma_i32_16x16x64_i8 v[42:45], v[142:145], v[178:181], v[42:45]
	v_mfma_i32_16x16x64_i8 v[38:41], v[146:149], v[182:185], 0
	s_nop 0
	v_mfma_i32_16x16x64_i8 v[38:41], v[138:141], v[178:181], v[38:41]
	v_mfma_i32_16x16x64_i8 v[46:49], v[134:137], v[182:185], 0
	s_nop 0
	v_mfma_i32_16x16x64_i8 v[46:49], v[130:133], v[178:181], v[46:49]
	v_mfma_i32_16x16x64_i8 v[58:61], v[158:161], v[174:177], 0
	s_nop 0
	v_mfma_i32_16x16x64_i8 v[58:61], v[154:157], v[170:173], v[58:61]
	v_mfma_i32_16x16x64_i8 v[74:77], v[150:153], v[174:177], 0
	s_nop 0
	v_mfma_i32_16x16x64_i8 v[74:77], v[142:145], v[170:173], v[74:77]
	v_mfma_i32_16x16x64_i8 v[70:73], v[146:149], v[174:177], 0
	s_nop 0
	v_mfma_i32_16x16x64_i8 v[70:73], v[138:141], v[170:173], v[70:73]
	v_mfma_i32_16x16x64_i8 v[78:81], v[134:137], v[174:177], 0
	s_nop 0
	v_mfma_i32_16x16x64_i8 v[78:81], v[130:133], v[170:173], v[78:81]
	v_mfma_i32_16x16x64_i8 v[90:93], v[158:161], v[166:169], 0
	s_nop 0
	v_mfma_i32_16x16x64_i8 v[90:93], v[154:157], v[162:165], v[90:93]
	v_mfma_i32_16x16x64_i8 v[106:109], v[150:153], v[166:169], 0
	s_nop 0
	v_mfma_i32_16x16x64_i8 v[106:109], v[142:145], v[162:165], v[106:109]
	v_mfma_i32_16x16x64_i8 v[102:105], v[146:149], v[166:169], 0
	s_nop 0
	v_mfma_i32_16x16x64_i8 v[102:105], v[138:141], v[162:165], v[102:105]
	v_mfma_i32_16x16x64_i8 v[110:113], v[134:137], v[166:169], 0
	s_nop 0
	v_mfma_i32_16x16x64_i8 v[110:113], v[130:133], v[162:165], v[110:113]
	s_setprio 0
	s_barrier
	s_add_u32 s45, s45, 0x100
	s_addc_u32 s78, s80, 0
	s_and_b64 s[66:67], s[76:77], exec
	s_cselect_b32 s67, s53, s78
	s_cselect_b32 s66, s52, s45
	s_add_u32 s52, s64, 0x80
	s_addc_u32 s53, s65, 0
	s_add_i32 s45, 0, 0x18000
	s_add_i32 s78, 0, 0x1c000
	v_add_u32_e32 v130, s45, v206
	v_add_u32_e32 v131, s78, v206
	ds_read_b128 v[158:161], v130
	ds_read_b128 v[154:157], v130 offset:1024
	ds_read_b128 v[150:153], v130 offset:2048
	ds_read_b128 v[146:149], v130 offset:3072
	ds_read_b128 v[142:145], v131
	ds_read_b128 v[138:141], v131 offset:1024
	ds_read_b128 v[134:137], v131 offset:2048
	ds_read_b128 v[130:133], v131 offset:3072
	s_mov_b64 s[76:77], s[66:67]
	v_mov_b32_e32 v209, v201
	s_mov_b32 m0, s1
	s_waitcnt lgkmcnt(0)
	ds_read_b128 v[162:165], v207 offset:32768
	ds_read_b128 v[166:169], v207 offset:33792
	ds_read_b128 v[170:173], v207 offset:34816
	ds_read_b128 v[174:177], v207 offset:35840
	ds_read_b128 v[178:181], v207 offset:36864
	ds_read_b128 v[182:185], v207 offset:37888
	ds_read_b128 v[186:189], v207 offset:38912
	ds_read_b128 v[190:193], v207 offset:39936
	s_add_u32 s66, s66, 0x40000
	global_load_lds_dwordx4 v209, s[76:77]
	v_mov_b32_e32 v209, v203
	s_mov_b32 m0, s61
	s_addc_u32 s67, s67, 0
	global_load_lds_dwordx4 v209, s[76:77]
	v_mov_b32_e32 v209, v201
	s_mov_b32 m0, s62
	s_nop 0
	global_load_lds_dwordx4 v209, s[66:67]
	v_mov_b32_e32 v209, v203
	s_mov_b32 m0, s63
	s_nop 0
	global_load_lds_dwordx4 v209, s[66:67]
	s_waitcnt vmcnt(20)
	s_waitcnt lgkmcnt(0)
	s_barrier
	s_setprio 1
	s_waitcnt lgkmcnt(0)
	v_mfma_i32_16x16x64_i8 v[18:21], v[158:161], v[162:165], v[18:21]
	s_nop 0
	v_mfma_i32_16x16x64_i8 v[18:21], v[154:157], v[166:169], v[18:21]
	v_mfma_i32_16x16x64_i8 v[22:25], v[150:153], v[162:165], v[22:25]
	s_nop 0
	v_mfma_i32_16x16x64_i8 v[22:25], v[146:149], v[166:169], v[22:25]
	v_mfma_i32_16x16x64_i8 v[26:29], v[142:145], v[162:165], v[26:29]
	s_nop 0
	v_mfma_i32_16x16x64_i8 v[26:29], v[138:141], v[166:169], v[26:29]
	v_mfma_i32_16x16x64_i8 v[34:37], v[134:137], v[162:165], v[34:37]
	s_nop 0
	v_mfma_i32_16x16x64_i8 v[34:37], v[130:133], v[166:169], v[34:37]
	v_mfma_i32_16x16x64_i8 v[50:53], v[158:161], v[170:173], v[50:53]
	s_nop 0
	v_mfma_i32_16x16x64_i8 v[50:53], v[154:157], v[174:177], v[50:53]
	v_mfma_i32_16x16x64_i8 v[62:65], v[150:153], v[170:173], v[62:65]
	s_nop 0
	v_mfma_i32_16x16x64_i8 v[62:65], v[146:149], v[174:177], v[62:65]
	v_mfma_i32_16x16x64_i8 v[54:57], v[142:145], v[170:173], v[54:57]
	s_nop 0
	v_mfma_i32_16x16x64_i8 v[54:57], v[138:141], v[174:177], v[54:57]
	v_mfma_i32_16x16x64_i8 v[66:69], v[134:137], v[170:173], v[66:69]
	s_nop 0
	v_mfma_i32_16x16x64_i8 v[66:69], v[130:133], v[174:177], v[66:69]
	v_mfma_i32_16x16x64_i8 v[82:85], v[158:161], v[178:181], v[82:85]
	s_nop 0
	v_mfma_i32_16x16x64_i8 v[82:85], v[154:157], v[182:185], v[82:85]
	v_mfma_i32_16x16x64_i8 v[94:97], v[150:153], v[178:181], v[94:97]
	s_nop 0
	v_mfma_i32_16x16x64_i8 v[94:97], v[146:149], v[182:185], v[94:97]
	v_mfma_i32_16x16x64_i8 v[86:89], v[142:145], v[178:181], v[86:89]
	s_nop 0
	v_mfma_i32_16x16x64_i8 v[86:89], v[138:141], v[182:185], v[86:89]
	v_mfma_i32_16x16x64_i8 v[98:101], v[134:137], v[178:181], v[98:101]
	s_nop 0
	v_mfma_i32_16x16x64_i8 v[98:101], v[130:133], v[182:185], v[98:101]
	v_mfma_i32_16x16x64_i8 v[114:117], v[158:161], v[186:189], v[114:117]
	s_nop 0
	v_mfma_i32_16x16x64_i8 v[114:117], v[154:157], v[190:193], v[114:117]
	v_mfma_i32_16x16x64_i8 v[122:125], v[150:153], v[186:189], v[122:125]
	s_nop 0
	v_mfma_i32_16x16x64_i8 v[122:125], v[146:149], v[190:193], v[122:125]
	v_mfma_i32_16x16x64_i8 v[118:121], v[142:145], v[186:189], v[118:121]
	s_nop 0
	v_mfma_i32_16x16x64_i8 v[118:121], v[138:141], v[190:193], v[118:121]
	v_mfma_i32_16x16x64_i8 v[126:129], v[134:137], v[186:189], v[126:129]
	s_nop 0
	v_mfma_i32_16x16x64_i8 v[126:129], v[130:133], v[190:193], v[126:129]
	s_setprio 0
	s_barrier
	v_mov_b32_e32 v209, v202
	s_add_i32 s45, s45, s10
	ds_read_b128 v[162:165], v207 offset:49152
	ds_read_b128 v[166:169], v207 offset:50176
	ds_read_b128 v[170:173], v207 offset:51200
	ds_read_b128 v[174:177], v207 offset:52224
	ds_read_b128 v[178:181], v207 offset:53248
	ds_read_b128 v[182:185], v207 offset:54272
	ds_read_b128 v[186:189], v207 offset:55296
	ds_read_b128 v[190:193], v207 offset:56320
	s_mov_b32 m0, s45
	s_nop 0
	global_load_lds_dwordx4 v209, s[52:53]
	v_mov_b32_e32 v209, v204
	s_add_i32 m0, s45, 0x2000
	s_nop 0
	global_load_lds_dwordx4 v209, s[52:53]
	s_add_u32 s52, s64, 0x40080
	s_addc_u32 s53, s65, 0
	v_mov_b32_e32 v209, v202
	s_add_i32 s45, s78, s10
	s_mov_b32 m0, s45
	s_nop 0
	global_load_lds_dwordx4 v209, s[52:53]
	v_mov_b32_e32 v209, v204
	s_add_i32 m0, s45, 0x2000
	s_nop 0
	global_load_lds_dwordx4 v209, s[52:53]
	s_waitcnt vmcnt(6)
	s_waitcnt lgkmcnt(0)
	s_barrier
	s_setprio 1
	s_waitcnt lgkmcnt(0)
	v_mfma_i32_16x16x64_i8 v[2:5], v[158:161], v[162:165], v[2:5]
	s_nop 0
	v_mfma_i32_16x16x64_i8 v[2:5], v[154:157], v[166:169], v[2:5]
	v_mfma_i32_16x16x64_i8 v[6:9], v[150:153], v[162:165], v[6:9]
	s_nop 0
	v_mfma_i32_16x16x64_i8 v[6:9], v[146:149], v[166:169], v[6:9]
	v_mfma_i32_16x16x64_i8 v[10:13], v[142:145], v[162:165], v[10:13]
	s_nop 0
	v_mfma_i32_16x16x64_i8 v[10:13], v[138:141], v[166:169], v[10:13]
	v_mfma_i32_16x16x64_i8 v[14:17], v[134:137], v[162:165], v[14:17]
	s_nop 0
	v_mfma_i32_16x16x64_i8 v[14:17], v[130:133], v[166:169], v[14:17]
	v_mfma_i32_16x16x64_i8 v[30:33], v[158:161], v[170:173], v[30:33]
	s_nop 0
	v_mfma_i32_16x16x64_i8 v[30:33], v[154:157], v[174:177], v[30:33]
	v_mfma_i32_16x16x64_i8 v[42:45], v[150:153], v[170:173], v[42:45]
	s_nop 0
	v_mfma_i32_16x16x64_i8 v[42:45], v[146:149], v[174:177], v[42:45]
	v_mfma_i32_16x16x64_i8 v[38:41], v[142:145], v[170:173], v[38:41]
	s_nop 0
	v_mfma_i32_16x16x64_i8 v[38:41], v[138:141], v[174:177], v[38:41]
	v_mfma_i32_16x16x64_i8 v[46:49], v[134:137], v[170:173], v[46:49]
	s_nop 0
	v_mfma_i32_16x16x64_i8 v[46:49], v[130:133], v[174:177], v[46:49]
	v_mfma_i32_16x16x64_i8 v[58:61], v[158:161], v[178:181], v[58:61]
	s_nop 0
	v_mfma_i32_16x16x64_i8 v[58:61], v[154:157], v[182:185], v[58:61]
	v_mfma_i32_16x16x64_i8 v[74:77], v[150:153], v[178:181], v[74:77]
	s_nop 0
	v_mfma_i32_16x16x64_i8 v[74:77], v[146:149], v[182:185], v[74:77]
	v_mfma_i32_16x16x64_i8 v[70:73], v[142:145], v[178:181], v[70:73]
	s_nop 0
	v_mfma_i32_16x16x64_i8 v[70:73], v[138:141], v[182:185], v[70:73]
	v_mfma_i32_16x16x64_i8 v[78:81], v[134:137], v[178:181], v[78:81]
	s_nop 0
	v_mfma_i32_16x16x64_i8 v[78:81], v[130:133], v[182:185], v[78:81]
	v_mfma_i32_16x16x64_i8 v[90:93], v[158:161], v[186:189], v[90:93]
	s_nop 0
	v_mfma_i32_16x16x64_i8 v[90:93], v[154:157], v[190:193], v[90:93]
	v_mfma_i32_16x16x64_i8 v[106:109], v[150:153], v[186:189], v[106:109]
	s_nop 0
	v_mfma_i32_16x16x64_i8 v[106:109], v[146:149], v[190:193], v[106:109]
	v_mfma_i32_16x16x64_i8 v[102:105], v[142:145], v[186:189], v[102:105]
	s_nop 0
	v_mfma_i32_16x16x64_i8 v[102:105], v[138:141], v[190:193], v[102:105]
	v_mfma_i32_16x16x64_i8 v[110:113], v[134:137], v[186:189], v[110:113]
	s_nop 0
	v_mfma_i32_16x16x64_i8 v[110:113], v[130:133], v[190:193], v[110:113]
	s_setprio 0
	s_barrier
	s_add_i32 s43, s43, 2
	s_add_u32 s50, s50, 0x100
	s_addc_u32 s51, s51, 0
	s_cmp_gt_u32 s43, 13
	s_cbranch_scc1 .LBB0_861
	s_mov_b64 s[64:65], s[8:9]
	s_mov_b64 s[52:53], s[26:27]

.LBB0_1088:
	s_waitcnt vmcnt(8)
	s_waitcnt lgkmcnt(0)
	s_barrier
	s_setprio 1
	v_mfma_i32_16x16x64_i8 v[18:21], v[158:161], v[190:193], 0
	s_nop 0
	v_mfma_i32_16x16x64_i8 v[18:21], v[154:157], v[186:189], v[18:21]
	v_mfma_i32_16x16x64_i8 v[22:25], v[150:153], v[190:193], 0
	s_nop 0
	v_mfma_i32_16x16x64_i8 v[22:25], v[142:145], v[186:189], v[22:25]
	v_mfma_i32_16x16x64_i8 v[26:29], v[146:149], v[190:193], 0
	s_nop 0
	v_mfma_i32_16x16x64_i8 v[26:29], v[138:141], v[186:189], v[26:29]
	v_mfma_i32_16x16x64_i8 v[34:37], v[134:137], v[190:193], 0
	s_nop 0
	v_mfma_i32_16x16x64_i8 v[34:37], v[130:133], v[186:189], v[34:37]
	v_mfma_i32_16x16x64_i8 v[50:53], v[158:161], v[182:185], 0
	s_nop 0
	v_mfma_i32_16x16x64_i8 v[50:53], v[154:157], v[178:181], v[50:53]
	v_mfma_i32_16x16x64_i8 v[62:65], v[150:153], v[182:185], 0
	s_nop 0
	v_mfma_i32_16x16x64_i8 v[62:65], v[142:145], v[178:181], v[62:65]
	v_mfma_i32_16x16x64_i8 v[54:57], v[146:149], v[182:185], 0
	s_nop 0
	v_mfma_i32_16x16x64_i8 v[54:57], v[138:141], v[178:181], v[54:57]
	v_mfma_i32_16x16x64_i8 v[66:69], v[134:137], v[182:185], 0
	s_nop 0
	v_mfma_i32_16x16x64_i8 v[66:69], v[130:133], v[178:181], v[66:69]
	v_mfma_i32_16x16x64_i8 v[82:85], v[158:161], v[174:177], 0
	s_nop 0
	v_mfma_i32_16x16x64_i8 v[82:85], v[154:157], v[170:173], v[82:85]
	v_mfma_i32_16x16x64_i8 v[94:97], v[150:153], v[174:177], 0
	s_nop 0
	v_mfma_i32_16x16x64_i8 v[94:97], v[142:145], v[170:173], v[94:97]
	v_mfma_i32_16x16x64_i8 v[86:89], v[146:149], v[174:177], 0
	s_nop 0
	v_mfma_i32_16x16x64_i8 v[86:89], v[138:141], v[170:173], v[86:89]
	v_mfma_i32_16x16x64_i8 v[98:101], v[134:137], v[174:177], 0
	s_nop 0
	v_mfma_i32_16x16x64_i8 v[98:101], v[130:133], v[170:173], v[98:101]
	v_mfma_i32_16x16x64_i8 v[114:117], v[158:161], v[166:169], 0
	s_nop 0
	v_mfma_i32_16x16x64_i8 v[114:117], v[154:157], v[162:165], v[114:117]
	v_mfma_i32_16x16x64_i8 v[122:125], v[150:153], v[166:169], 0
	s_nop 0
	v_mfma_i32_16x16x64_i8 v[122:125], v[142:145], v[162:165], v[122:125]
	v_mfma_i32_16x16x64_i8 v[118:121], v[146:149], v[166:169], 0
	s_nop 0
	v_mfma_i32_16x16x64_i8 v[118:121], v[138:141], v[162:165], v[118:121]
	v_mfma_i32_16x16x64_i8 v[126:129], v[134:137], v[166:169], 0
	s_nop 0
	v_mfma_i32_16x16x64_i8 v[126:129], v[130:133], v[162:165], v[126:129]
	s_setprio 0
	s_barrier
	s_add_u32 s81, s77, s48
	s_addc_u32 s82, s78, s49
	s_cmp_eq_u32 s41, 12
	s_cselect_b64 s[66:67], -1, 0
	s_and_b64 s[74:75], s[66:67], exec
	s_cselect_b32 s53, s53, s82
	s_cselect_b32 s52, s52, s81
	s_mov_b64 s[74:75], s[52:53]
	v_mov_b32_e32 v205, v197
	s_mov_b32 m0, s33
	s_waitcnt lgkmcnt(0)
	ds_read_b128 v[190:193], v204 offset:16384
	ds_read_b128 v[186:189], v204 offset:17408
	ds_read_b128 v[182:185], v204 offset:18432
	ds_read_b128 v[178:181], v204 offset:19456
	ds_read_b128 v[174:177], v204 offset:20480
	ds_read_b128 v[170:173], v204 offset:21504
	ds_read_b128 v[166:169], v204 offset:22528
	ds_read_b128 v[162:165], v204 offset:23552
	s_nop 0
	global_load_lds_dwordx4 v205, s[74:75]
	v_mov_b32_e32 v205, v199
	s_mov_b32 m0, s35
	s_nop 0
	global_load_lds_dwordx4 v205, s[74:75]
	s_add_u32 s74, s52, 0x40000
	s_addc_u32 s75, s53, 0
	v_mov_b32_e32 v205, v197
	s_mov_b32 m0, s60
	s_nop 0
	global_load_lds_dwordx4 v205, s[74:75]
	v_mov_b32_e32 v205, v199
	s_mov_b32 m0, s61
	s_nop 0
	global_load_lds_dwordx4 v205, s[74:75]
	v_lshl_or_b32 v242, s79, 8, v203
	v_lshl_add_u32 v240, s76, 8, v201
	v_ashrrev_i32_e32 v243, 31, v242
	v_ashrrev_i32_e32 v241, 31, v240
	v_lshl_add_u64 v[242:243], v[242:243], 2, s[8:9]
	v_lshl_add_u64 v[240:241], v[240:241], 2, s[38:39]
	global_load_dwordx4 v[210:213], v[242:243], off
	global_load_dwordx4 v[214:217], v[242:243], off offset:16
	global_load_dwordx4 v[218:221], v[242:243], off offset:512
	global_load_dwordx4 v[222:225], v[242:243], off offset:528
	global_load_dword v232, v[240:241], off
	global_load_dword v233, v[240:241], off offset:64
	global_load_dword v234, v[240:241], off offset:128
	global_load_dword v235, v[240:241], off offset:192
	global_load_dword v236, v[240:241], off offset:512
	global_load_dword v237, v[240:241], off offset:576
	global_load_dword v238, v[240:241], off offset:640
	global_load_dword v239, v[240:241], off offset:704
	s_waitcnt vmcnt(18)
	s_waitcnt lgkmcnt(0)
	s_barrier
	s_setprio 1
	v_mfma_i32_16x16x64_i8 v[2:5], v[158:161], v[190:193], 0
	s_nop 0
	v_mfma_i32_16x16x64_i8 v[2:5], v[154:157], v[186:189], v[2:5]
	v_mfma_i32_16x16x64_i8 v[6:9], v[150:153], v[190:193], 0
	s_nop 0
	v_mfma_i32_16x16x64_i8 v[6:9], v[142:145], v[186:189], v[6:9]
	v_mfma_i32_16x16x64_i8 v[10:13], v[146:149], v[190:193], 0
	s_nop 0
	v_mfma_i32_16x16x64_i8 v[10:13], v[138:141], v[186:189], v[10:13]
	v_mfma_i32_16x16x64_i8 v[14:17], v[134:137], v[190:193], 0
	s_nop 0
	v_mfma_i32_16x16x64_i8 v[14:17], v[130:133], v[186:189], v[14:17]
	v_mfma_i32_16x16x64_i8 v[30:33], v[158:161], v[182:185], 0
	s_nop 0
	v_mfma_i32_16x16x64_i8 v[30:33], v[154:157], v[178:181], v[30:33]
	v_mfma_i32_16x16x64_i8 v[42:45], v[150:153], v[182:185], 0
	s_nop 0
	v_mfma_i32_16x16x64_i8 v[42:45], v[142:145], v[178:181], v[42:45]
	v_mfma_i32_16x16x64_i8 v[38:41], v[146:149], v[182:185], 0
	s_nop 0
	v_mfma_i32_16x16x64_i8 v[38:41], v[138:141], v[178:181], v[38:41]
	v_mfma_i32_16x16x64_i8 v[46:49], v[134:137], v[182:185], 0
	s_nop 0
	v_mfma_i32_16x16x64_i8 v[46:49], v[130:133], v[178:181], v[46:49]
	v_mfma_i32_16x16x64_i8 v[58:61], v[158:161], v[174:177], 0
	s_nop 0
	v_mfma_i32_16x16x64_i8 v[58:61], v[154:157], v[170:173], v[58:61]
	v_mfma_i32_16x16x64_i8 v[74:77], v[150:153], v[174:177], 0
	s_nop 0
	v_mfma_i32_16x16x64_i8 v[74:77], v[142:145], v[170:173], v[74:77]
	v_mfma_i32_16x16x64_i8 v[70:73], v[146:149], v[174:177], 0
	s_nop 0
	v_mfma_i32_16x16x64_i8 v[70:73], v[138:141], v[170:173], v[70:73]
	v_mfma_i32_16x16x64_i8 v[78:81], v[134:137], v[174:177], 0
	s_nop 0
	v_mfma_i32_16x16x64_i8 v[78:81], v[130:133], v[170:173], v[78:81]
	v_mfma_i32_16x16x64_i8 v[90:93], v[158:161], v[166:169], 0
	s_nop 0
	v_mfma_i32_16x16x64_i8 v[90:93], v[154:157], v[162:165], v[90:93]
	v_mfma_i32_16x16x64_i8 v[106:109], v[150:153], v[166:169], 0
	s_nop 0
	v_mfma_i32_16x16x64_i8 v[106:109], v[142:145], v[162:165], v[106:109]
	v_mfma_i32_16x16x64_i8 v[102:105], v[146:149], v[166:169], 0
	s_nop 0
	v_mfma_i32_16x16x64_i8 v[102:105], v[138:141], v[162:165], v[102:105]
	v_mfma_i32_16x16x64_i8 v[110:113], v[134:137], v[166:169], 0
	s_nop 0
	v_mfma_i32_16x16x64_i8 v[110:113], v[130:133], v[162:165], v[110:113]
	s_setprio 0
	s_barrier
	s_add_u32 s43, s43, 0x100
	s_addc_u32 s74, s80, 0
	s_and_b64 s[64:65], s[66:67], exec
	s_cselect_b32 s65, s51, s74
	s_cselect_b32 s64, s50, s43
	s_add_u32 s50, s52, 0x80
	s_addc_u32 s51, s53, 0
	s_add_i32 s43, 0, 0x18000
	s_add_i32 s74, 0, 0x1c000
	v_add_u32_e32 v130, s43, v202
	v_add_u32_e32 v131, s74, v202
	ds_read_b128 v[158:161], v130
	ds_read_b128 v[154:157], v130 offset:1024
	ds_read_b128 v[150:153], v130 offset:2048
	ds_read_b128 v[146:149], v130 offset:3072
	ds_read_b128 v[142:145], v131
	ds_read_b128 v[138:141], v131 offset:1024
	ds_read_b128 v[134:137], v131 offset:2048
	ds_read_b128 v[130:133], v131 offset:3072
	s_mov_b64 s[66:67], s[64:65]
	v_mov_b32_e32 v205, v196
	s_mov_b32 m0, s5
	s_waitcnt lgkmcnt(0)
	ds_read_b128 v[162:165], v204 offset:32768
	ds_read_b128 v[166:169], v204 offset:33792
	ds_read_b128 v[170:173], v204 offset:34816
	ds_read_b128 v[174:177], v204 offset:35840
	ds_read_b128 v[178:181], v204 offset:36864
	ds_read_b128 v[182:185], v204 offset:37888
	ds_read_b128 v[186:189], v204 offset:38912
	ds_read_b128 v[190:193], v204 offset:39936
	s_add_u32 s64, s64, 0x40000
	global_load_lds_dwordx4 v205, s[66:67]
	v_mov_b32_e32 v205, v198
	s_mov_b32 m0, s62
	s_addc_u32 s65, s65, 0
	global_load_lds_dwordx4 v205, s[66:67]
	v_mov_b32_e32 v205, v196
	s_mov_b32 m0, s63
	s_nop 0
	global_load_lds_dwordx4 v205, s[64:65]
	v_mov_b32_e32 v205, v198
	s_mov_b32 m0, s69
	s_nop 0
	global_load_lds_dwordx4 v205, s[64:65]
	s_waitcnt vmcnt(20)
	s_waitcnt lgkmcnt(0)
	s_barrier
	s_setprio 1
	s_waitcnt lgkmcnt(0)
	v_mfma_i32_16x16x64_i8 v[18:21], v[158:161], v[162:165], v[18:21]
	s_nop 0
	v_mfma_i32_16x16x64_i8 v[18:21], v[154:157], v[166:169], v[18:21]
	v_mfma_i32_16x16x64_i8 v[22:25], v[150:153], v[162:165], v[22:25]
	s_nop 0
	v_mfma_i32_16x16x64_i8 v[22:25], v[146:149], v[166:169], v[22:25]
	v_mfma_i32_16x16x64_i8 v[26:29], v[142:145], v[162:165], v[26:29]
	s_nop 0
	v_mfma_i32_16x16x64_i8 v[26:29], v[138:141], v[166:169], v[26:29]
	v_mfma_i32_16x16x64_i8 v[34:37], v[134:137], v[162:165], v[34:37]
	s_nop 0
	v_mfma_i32_16x16x64_i8 v[34:37], v[130:133], v[166:169], v[34:37]
	v_mfma_i32_16x16x64_i8 v[50:53], v[158:161], v[170:173], v[50:53]
	s_nop 0
	v_mfma_i32_16x16x64_i8 v[50:53], v[154:157], v[174:177], v[50:53]
	v_mfma_i32_16x16x64_i8 v[62:65], v[150:153], v[170:173], v[62:65]
	s_nop 0
	v_mfma_i32_16x16x64_i8 v[62:65], v[146:149], v[174:177], v[62:65]
	v_mfma_i32_16x16x64_i8 v[54:57], v[142:145], v[170:173], v[54:57]
	s_nop 0
	v_mfma_i32_16x16x64_i8 v[54:57], v[138:141], v[174:177], v[54:57]
	v_mfma_i32_16x16x64_i8 v[66:69], v[134:137], v[170:173], v[66:69]
	s_nop 0
	v_mfma_i32_16x16x64_i8 v[66:69], v[130:133], v[174:177], v[66:69]
	v_mfma_i32_16x16x64_i8 v[82:85], v[158:161], v[178:181], v[82:85]
	s_nop 0
	v_mfma_i32_16x16x64_i8 v[82:85], v[154:157], v[182:185], v[82:85]
	v_mfma_i32_16x16x64_i8 v[94:97], v[150:153], v[178:181], v[94:97]
	s_nop 0
	v_mfma_i32_16x16x64_i8 v[94:97], v[146:149], v[182:185], v[94:97]
	v_mfma_i32_16x16x64_i8 v[86:89], v[142:145], v[178:181], v[86:89]
	s_nop 0
	v_mfma_i32_16x16x64_i8 v[86:89], v[138:141], v[182:185], v[86:89]
	v_mfma_i32_16x16x64_i8 v[98:101], v[134:137], v[178:181], v[98:101]
	s_nop 0
	v_mfma_i32_16x16x64_i8 v[98:101], v[130:133], v[182:185], v[98:101]
	v_mfma_i32_16x16x64_i8 v[114:117], v[158:161], v[186:189], v[114:117]
	s_nop 0
	v_mfma_i32_16x16x64_i8 v[114:117], v[154:157], v[190:193], v[114:117]
	v_mfma_i32_16x16x64_i8 v[122:125], v[150:153], v[186:189], v[122:125]
	s_nop 0
	v_mfma_i32_16x16x64_i8 v[122:125], v[146:149], v[190:193], v[122:125]
	v_mfma_i32_16x16x64_i8 v[118:121], v[142:145], v[186:189], v[118:121]
	s_nop 0
	v_mfma_i32_16x16x64_i8 v[118:121], v[138:141], v[190:193], v[118:121]
	v_mfma_i32_16x16x64_i8 v[126:129], v[134:137], v[186:189], v[126:129]
	s_nop 0
	v_mfma_i32_16x16x64_i8 v[126:129], v[130:133], v[190:193], v[126:129]
	s_setprio 0
	s_barrier
	v_mov_b32_e32 v205, v197
	s_add_i32 s43, s43, s10
	ds_read_b128 v[162:165], v204 offset:49152
	ds_read_b128 v[166:169], v204 offset:50176
	ds_read_b128 v[170:173], v204 offset:51200
	ds_read_b128 v[174:177], v204 offset:52224
	ds_read_b128 v[178:181], v204 offset:53248
	ds_read_b128 v[182:185], v204 offset:54272
	ds_read_b128 v[186:189], v204 offset:55296
	ds_read_b128 v[190:193], v204 offset:56320
	s_mov_b32 m0, s43
	s_nop 0
	global_load_lds_dwordx4 v205, s[50:51]
	v_mov_b32_e32 v205, v199
	s_add_i32 m0, s43, 0x2000
	s_nop 0
	global_load_lds_dwordx4 v205, s[50:51]
	s_add_u32 s50, s52, 0x40080
	s_addc_u32 s51, s53, 0
	v_mov_b32_e32 v205, v197
	s_add_i32 s43, s74, s10
	s_mov_b32 m0, s43
	s_nop 0
	global_load_lds_dwordx4 v205, s[50:51]
	v_mov_b32_e32 v205, v199
	s_add_i32 m0, s43, 0x2000
	s_nop 0
	global_load_lds_dwordx4 v205, s[50:51]
	s_waitcnt vmcnt(6)
	s_waitcnt lgkmcnt(0)
	s_barrier
	s_setprio 1
	s_waitcnt lgkmcnt(0)
	v_mfma_i32_16x16x64_i8 v[2:5], v[158:161], v[162:165], v[2:5]
	s_nop 0
	v_mfma_i32_16x16x64_i8 v[2:5], v[154:157], v[166:169], v[2:5]
	v_mfma_i32_16x16x64_i8 v[6:9], v[150:153], v[162:165], v[6:9]
	s_nop 0
	v_mfma_i32_16x16x64_i8 v[6:9], v[146:149], v[166:169], v[6:9]
	v_mfma_i32_16x16x64_i8 v[10:13], v[142:145], v[162:165], v[10:13]
	s_nop 0
	v_mfma_i32_16x16x64_i8 v[10:13], v[138:141], v[166:169], v[10:13]
	v_mfma_i32_16x16x64_i8 v[14:17], v[134:137], v[162:165], v[14:17]
	s_nop 0
	v_mfma_i32_16x16x64_i8 v[14:17], v[130:133], v[166:169], v[14:17]
	v_mfma_i32_16x16x64_i8 v[30:33], v[158:161], v[170:173], v[30:33]
	s_nop 0
	v_mfma_i32_16x16x64_i8 v[30:33], v[154:157], v[174:177], v[30:33]
	v_mfma_i32_16x16x64_i8 v[42:45], v[150:153], v[170:173], v[42:45]
	s_nop 0
	v_mfma_i32_16x16x64_i8 v[42:45], v[146:149], v[174:177], v[42:45]
	v_mfma_i32_16x16x64_i8 v[38:41], v[142:145], v[170:173], v[38:41]
	s_nop 0
	v_mfma_i32_16x16x64_i8 v[38:41], v[138:141], v[174:177], v[38:41]
	v_mfma_i32_16x16x64_i8 v[46:49], v[134:137], v[170:173], v[46:49]
	s_nop 0
	v_mfma_i32_16x16x64_i8 v[46:49], v[130:133], v[174:177], v[46:49]
	v_mfma_i32_16x16x64_i8 v[58:61], v[158:161], v[178:181], v[58:61]
	s_nop 0
	v_mfma_i32_16x16x64_i8 v[58:61], v[154:157], v[182:185], v[58:61]
	v_mfma_i32_16x16x64_i8 v[74:77], v[150:153], v[178:181], v[74:77]
	s_nop 0
	v_mfma_i32_16x16x64_i8 v[74:77], v[146:149], v[182:185], v[74:77]
	v_mfma_i32_16x16x64_i8 v[70:73], v[142:145], v[178:181], v[70:73]
	s_nop 0
	v_mfma_i32_16x16x64_i8 v[70:73], v[138:141], v[182:185], v[70:73]
	v_mfma_i32_16x16x64_i8 v[78:81], v[134:137], v[178:181], v[78:81]
	s_nop 0
	v_mfma_i32_16x16x64_i8 v[78:81], v[130:133], v[182:185], v[78:81]
	v_mfma_i32_16x16x64_i8 v[90:93], v[158:161], v[186:189], v[90:93]
	s_nop 0
	v_mfma_i32_16x16x64_i8 v[90:93], v[154:157], v[190:193], v[90:93]
	v_mfma_i32_16x16x64_i8 v[106:109], v[150:153], v[186:189], v[106:109]
	s_nop 0
	v_mfma_i32_16x16x64_i8 v[106:109], v[146:149], v[190:193], v[106:109]
	v_mfma_i32_16x16x64_i8 v[102:105], v[142:145], v[186:189], v[102:105]
	s_nop 0
	v_mfma_i32_16x16x64_i8 v[102:105], v[138:141], v[190:193], v[102:105]
	v_mfma_i32_16x16x64_i8 v[110:113], v[134:137], v[186:189], v[110:113]
	s_nop 0
	v_mfma_i32_16x16x64_i8 v[110:113], v[130:133], v[190:193], v[110:113]
	s_setprio 0
	s_barrier
	s_add_i32 s41, s41, 2
	s_add_u32 s48, s48, 0x100
	s_addc_u32 s49, s49, 0
	s_cmp_gt_u32 s41, 13
	s_cbranch_scc1 .LBB0_1098
	s_mov_b64 s[52:53], s[14:15]
	s_mov_b64 s[50:51], s[26:27]
